# baseline (speedup 1.0000x reference)
.Lj_loop:
	s_and_b32 s70, s20, 1
	s_waitcnt lgkmcnt(0)
	s_barrier
	s_mul_i32 s38, s70, 0x1100
	s_lshl_b32 s10, s70, 13
	s_add_i32 s14, s10, s34
	s_mov_b32 s15, 0
	v_lshl_add_u64 v[244:245], v[192:193], 0, s[14:15]
	s_add_i32 s14, s10, s30
	v_lshl_add_u64 v[246:247], v[192:193], 0, s[14:15]
	s_add_i32 s14, s10, s28
	v_lshl_add_u64 v[248:249], v[192:193], 0, s[14:15]
	v_add_u32_e32 v229, s38, v222
	v_add_u32_e32 v230, s43, v229
	ds_read_b128 v[150:153], v230 offset:0
	ds_read_b128 v[194:197], v230 offset:128
	ds_read_b128 v[198:201], v230 offset:256
	ds_read_b128 v[232:235], v230 offset:384
	s_xor_b32 s83, s70, 1
	s_lshl_b32 s83, s83, 4
	s_add_i32 s83, s83, 0x26a20
	v_mov_b32_e32 v239, s83
	ds_read_b128 v[240:243], v239
	s_cmp_lg_u32 s20, 1
	s_cselect_b64 s[10:11], -1, 0
	s_and_b64 s[14:15], s[10:11], s[26:27]
	s_and_saveexec_b64 s[10:11], s[14:15]
	s_cbranch_execz .Lj_norr
	s_lshl_b32 s14, s70, 4
	s_or_b32 s14, s14, 0x26a00
	v_mov_b32_e32 v236, s14
	s_add_i32 s14, s20, -2
	ds_read_b128 v[236:239], v236
	s_cmp_lg_u32 s20, 0
	s_cselect_b32 s14, s14, 0x64
	s_ashr_i32 s15, s14, 31
	s_add_u32 s14, s22, s14
	s_addc_u32 s15, s23, s15
	s_lshl_b64 s[14:15], s[14:15], 4
	s_add_u32 s14, s24, s14
	s_addc_u32 s15, s25, s15
	s_waitcnt lgkmcnt(0)
	v_add_f32_e32 v236, v236, v237
	v_add_f32_e32 v238, v238, v239
	v_add_f32_e32 v236, v236, v238
	global_store_dword v191, v236, s[14:15]

.Lj_nostop:
	s_cmp_eq_u32 s20, 0
	s_cbranch_scc1 .Lj_nopollE
	global_load_dwordx2 v[214:215], v[244:245], off sc1
	global_load_dwordx2 v[210:211], v[246:247], off sc1
	global_load_dwordx2 v[212:213], v[248:249], off sc1
